# DSA select radix descent: compares into distinct SGPR pairs, popcounts one group behind (no VALU->SALU stall per pair); on top of v39
# speedup vs baseline: 1.0036x; 1.0016x over previous
.LBB0_821:
	s_add_i32 s0, s0, -1
	s_lshl_b32 s1, 1, s0
	s_or_b32 s1, s1, s9
	s_waitcnt lgkmcnt(0)
	v_cmp_le_u32_e64 s[14:15], s1, v90
	v_cmp_le_u32_e64 s[16:17], s1, v88
	v_cmp_le_u32_e64 s[18:19], s1, v89
	v_cmp_le_u32_e64 s[20:21], s1, v86
	v_cmp_le_u32_e64 s[22:23], s1, v87
	v_cmp_le_u32_e64 s[24:25], s1, v84
	v_cmp_le_u32_e64 s[26:27], s1, v85
	v_cmp_le_u32_e64 s[28:29], s1, v82
	v_cmp_le_u32_e64 s[30:31], s1, v83
	v_cmp_le_u32_e64 s[34:35], s1, v80
	v_cmp_le_u32_e64 s[36:37], s1, v81
	v_cmp_le_u32_e64 s[38:39], s1, v9
	s_bcnt1_i32_b64 s11, s[14:15]
	s_bcnt1_i32_b64 s12, s[16:17]
	s_add_i32 s11, s11, s12
	s_bcnt1_i32_b64 s12, s[18:19]
	s_add_i32 s11, s11, s12
	s_bcnt1_i32_b64 s12, s[20:21]
	s_add_i32 s11, s11, s12
	s_bcnt1_i32_b64 s12, s[22:23]
	s_add_i32 s11, s11, s12
	s_bcnt1_i32_b64 s12, s[24:25]
	s_add_i32 s11, s11, s12
	v_cmp_le_u32_e64 s[14:15], s1, v78
	v_cmp_le_u32_e64 s[16:17], s1, v7
	v_cmp_le_u32_e64 s[18:19], s1, v8
	v_cmp_le_u32_e64 s[20:21], s1, v5
	v_cmp_le_u32_e64 s[22:23], s1, v6
	v_cmp_le_u32_e64 s[24:25], s1, v3
	s_bcnt1_i32_b64 s12, s[26:27]
	s_add_i32 s11, s11, s12
	s_bcnt1_i32_b64 s12, s[28:29]
	s_add_i32 s11, s11, s12
	s_bcnt1_i32_b64 s12, s[30:31]
	s_add_i32 s11, s11, s12
	s_bcnt1_i32_b64 s12, s[34:35]
	s_add_i32 s11, s11, s12
	s_bcnt1_i32_b64 s12, s[36:37]
	s_add_i32 s11, s11, s12
	s_bcnt1_i32_b64 s12, s[38:39]
	s_add_i32 s11, s11, s12
	v_cmp_le_u32_e64 s[26:27], s1, v4
	v_cmp_le_u32_e64 s[28:29], s1, v2
	s_bcnt1_i32_b64 s12, s[14:15]
	s_add_i32 s11, s11, s12
	s_bcnt1_i32_b64 s12, s[16:17]
	s_add_i32 s11, s11, s12
	s_bcnt1_i32_b64 s12, s[18:19]
	s_add_i32 s11, s11, s12
	s_bcnt1_i32_b64 s12, s[20:21]
	s_add_i32 s11, s11, s12
	s_bcnt1_i32_b64 s12, s[22:23]
	s_add_i32 s11, s11, s12
	s_bcnt1_i32_b64 s12, s[24:25]
	s_add_i32 s11, s11, s12
	s_bcnt1_i32_b64 s12, s[26:27]
	s_add_i32 s11, s11, s12
	s_bcnt1_i32_b64 s12, s[28:29]
	s_add_i32 s11, s11, s12
	s_cmpk_gt_u32 s11, 0xff
	s_cselect_b32 s9, s1, s9
	s_cmp_lt_u32 s0, 17
	s_cbranch_scc0 .LBB0_821
	v_cmp_le_u32_e64 s[14:15], s9, v90
	v_cmp_le_u32_e64 s[16:17], s9, v88
	v_cmp_le_u32_e64 s[18:19], s9, v89
	v_cmp_le_u32_e64 s[20:21], s9, v86
	v_cmp_le_u32_e64 s[22:23], s9, v87
	v_cmp_le_u32_e64 s[24:25], s9, v84
	v_cmp_le_u32_e64 s[26:27], s9, v85
	v_cmp_le_u32_e64 s[28:29], s9, v82
	v_cmp_le_u32_e64 s[30:31], s9, v83
	v_cmp_le_u32_e64 s[34:35], s9, v80
	v_cmp_le_u32_e64 s[36:37], s9, v81
	v_cmp_le_u32_e64 s[38:39], s9, v9
	s_bcnt1_i32_b64 s0, s[14:15]
	s_bcnt1_i32_b64 s1, s[16:17]
	s_add_i32 s0, s0, s1
	s_bcnt1_i32_b64 s1, s[18:19]
	s_add_i32 s0, s0, s1
	s_bcnt1_i32_b64 s1, s[20:21]
	s_add_i32 s0, s0, s1
	s_bcnt1_i32_b64 s1, s[22:23]
	s_add_i32 s0, s0, s1
	s_bcnt1_i32_b64 s1, s[24:25]
	s_add_i32 s0, s0, s1
	v_cmp_le_u32_e64 s[14:15], s9, v78
	v_cmp_le_u32_e64 s[16:17], s9, v7
	v_cmp_le_u32_e64 s[18:19], s9, v8
	v_cmp_le_u32_e64 s[20:21], s9, v5
	v_cmp_le_u32_e64 s[22:23], s9, v6
	v_cmp_le_u32_e64 s[24:25], s9, v3
	s_bcnt1_i32_b64 s1, s[26:27]
	s_add_i32 s0, s0, s1
	s_bcnt1_i32_b64 s1, s[28:29]
	s_add_i32 s0, s0, s1
	s_bcnt1_i32_b64 s1, s[30:31]
	s_add_i32 s0, s0, s1
	s_bcnt1_i32_b64 s1, s[34:35]
	s_add_i32 s0, s0, s1
	s_bcnt1_i32_b64 s1, s[36:37]
	s_add_i32 s0, s0, s1
	s_bcnt1_i32_b64 s1, s[38:39]
	s_add_i32 s0, s0, s1
	v_cmp_le_u32_e64 s[26:27], s9, v4
	v_cmp_le_u32_e64 s[28:29], s9, v2
	s_bcnt1_i32_b64 s1, s[14:15]
	s_add_i32 s0, s0, s1
	s_bcnt1_i32_b64 s1, s[16:17]
	s_add_i32 s0, s0, s1
	s_bcnt1_i32_b64 s1, s[18:19]
	s_add_i32 s0, s0, s1
	s_bcnt1_i32_b64 s1, s[20:21]
	s_add_i32 s0, s0, s1
	s_bcnt1_i32_b64 s1, s[22:23]
	s_add_i32 s0, s0, s1
	s_bcnt1_i32_b64 s1, s[24:25]
	s_add_i32 s0, s0, s1
	s_bcnt1_i32_b64 s1, s[26:27]
	s_add_i32 s0, s0, s1
	s_bcnt1_i32_b64 s1, s[28:29]
	s_add_i32 s0, s0, s1
	s_cmpk_eq_i32 s0, 0x100
	s_cbranch_scc1 .LBB0_825
	s_mov_b32 s0, 15
.LBB0_824:
	s_lshl_b32 s1, 1, s0
	s_or_b32 s1, s1, s9
	v_cmp_le_u32_e64 s[14:15], s1, v90
	v_cmp_le_u32_e64 s[16:17], s1, v88
	v_cmp_le_u32_e64 s[18:19], s1, v89
	v_cmp_le_u32_e64 s[20:21], s1, v86
	v_cmp_le_u32_e64 s[22:23], s1, v87
	v_cmp_le_u32_e64 s[24:25], s1, v84
	v_cmp_le_u32_e64 s[26:27], s1, v85
	v_cmp_le_u32_e64 s[28:29], s1, v82
	v_cmp_le_u32_e64 s[30:31], s1, v83
	v_cmp_le_u32_e64 s[34:35], s1, v80
	v_cmp_le_u32_e64 s[36:37], s1, v81
	v_cmp_le_u32_e64 s[38:39], s1, v9
	s_bcnt1_i32_b64 s11, s[14:15]
	s_bcnt1_i32_b64 s12, s[16:17]
	s_add_i32 s11, s11, s12
	s_bcnt1_i32_b64 s12, s[18:19]
	s_add_i32 s11, s11, s12
	s_bcnt1_i32_b64 s12, s[20:21]
	s_add_i32 s11, s11, s12
	s_bcnt1_i32_b64 s12, s[22:23]
	s_add_i32 s11, s11, s12
	s_bcnt1_i32_b64 s12, s[24:25]
	s_add_i32 s11, s11, s12
	v_cmp_le_u32_e64 s[14:15], s1, v78
	v_cmp_le_u32_e64 s[16:17], s1, v7
	v_cmp_le_u32_e64 s[18:19], s1, v8
	v_cmp_le_u32_e64 s[20:21], s1, v5
	v_cmp_le_u32_e64 s[22:23], s1, v6
	v_cmp_le_u32_e64 s[24:25], s1, v3
	s_bcnt1_i32_b64 s12, s[26:27]
	s_add_i32 s11, s11, s12
	s_bcnt1_i32_b64 s12, s[28:29]
	s_add_i32 s11, s11, s12
	s_bcnt1_i32_b64 s12, s[30:31]
	s_add_i32 s11, s11, s12
	s_bcnt1_i32_b64 s12, s[34:35]
	s_add_i32 s11, s11, s12
	s_bcnt1_i32_b64 s12, s[36:37]
	s_add_i32 s11, s11, s12
	s_bcnt1_i32_b64 s12, s[38:39]
	s_add_i32 s11, s11, s12
	v_cmp_le_u32_e64 s[26:27], s1, v4
	v_cmp_le_u32_e64 s[28:29], s1, v2
	s_bcnt1_i32_b64 s12, s[14:15]
	s_add_i32 s11, s11, s12
	s_bcnt1_i32_b64 s12, s[16:17]
	s_add_i32 s11, s11, s12
	s_bcnt1_i32_b64 s12, s[18:19]
	s_add_i32 s11, s11, s12
	s_bcnt1_i32_b64 s12, s[20:21]
	s_add_i32 s11, s11, s12
	s_bcnt1_i32_b64 s12, s[22:23]
	s_add_i32 s11, s11, s12
	s_bcnt1_i32_b64 s12, s[24:25]
	s_add_i32 s11, s11, s12
	s_bcnt1_i32_b64 s12, s[26:27]
	s_add_i32 s11, s11, s12
	s_bcnt1_i32_b64 s12, s[28:29]
	s_add_i32 s11, s11, s12
	s_cmpk_gt_u32 s11, 0xff
	s_cselect_b32 s9, s1, s9
	s_add_i32 s0, s0, -1
	s_cmp_lg_u32 s0, -1
	s_cbranch_scc1 .LBB0_824

.LBB0_828:
	s_add_i32 s0, s0, -1
	s_lshl_b32 s1, 1, s0
	s_or_b32 s1, s1, s9
	s_waitcnt lgkmcnt(0)
	v_cmp_le_u32_e64 s[14:15], s1, v90
	v_cmp_le_u32_e64 s[16:17], s1, v88
	v_cmp_le_u32_e64 s[18:19], s1, v89
	v_cmp_le_u32_e64 s[20:21], s1, v86
	v_cmp_le_u32_e64 s[22:23], s1, v87
	v_cmp_le_u32_e64 s[24:25], s1, v84
	v_cmp_le_u32_e64 s[26:27], s1, v85
	v_cmp_le_u32_e64 s[28:29], s1, v82
	v_cmp_le_u32_e64 s[30:31], s1, v83
	v_cmp_le_u32_e64 s[34:35], s1, v80
	v_cmp_le_u32_e64 s[36:37], s1, v81
	v_cmp_le_u32_e64 s[38:39], s1, v9
	s_bcnt1_i32_b64 s11, s[14:15]
	s_bcnt1_i32_b64 s12, s[16:17]
	s_add_i32 s11, s11, s12
	s_bcnt1_i32_b64 s12, s[18:19]
	s_add_i32 s11, s11, s12
	s_bcnt1_i32_b64 s12, s[20:21]
	s_add_i32 s11, s11, s12
	s_bcnt1_i32_b64 s12, s[22:23]
	s_add_i32 s11, s11, s12
	s_bcnt1_i32_b64 s12, s[24:25]
	s_add_i32 s11, s11, s12
	v_cmp_le_u32_e64 s[14:15], s1, v78
	v_cmp_le_u32_e64 s[16:17], s1, v7
	v_cmp_le_u32_e64 s[18:19], s1, v8
	v_cmp_le_u32_e64 s[20:21], s1, v5
	s_bcnt1_i32_b64 s12, s[26:27]
	s_add_i32 s11, s11, s12
	s_bcnt1_i32_b64 s12, s[28:29]
	s_add_i32 s11, s11, s12
	s_bcnt1_i32_b64 s12, s[30:31]
	s_add_i32 s11, s11, s12
	s_bcnt1_i32_b64 s12, s[34:35]
	s_add_i32 s11, s11, s12
	s_bcnt1_i32_b64 s12, s[36:37]
	s_add_i32 s11, s11, s12
	s_bcnt1_i32_b64 s12, s[38:39]
	s_add_i32 s11, s11, s12
	s_bcnt1_i32_b64 s12, s[14:15]
	s_add_i32 s11, s11, s12
	s_bcnt1_i32_b64 s12, s[16:17]
	s_add_i32 s11, s11, s12
	s_bcnt1_i32_b64 s12, s[18:19]
	s_add_i32 s11, s11, s12
	s_bcnt1_i32_b64 s12, s[20:21]
	s_add_i32 s11, s11, s12
	s_cmpk_gt_u32 s11, 0xff
	s_cselect_b32 s9, s1, s9
	s_cmp_lt_u32 s0, 17
	s_cbranch_scc0 .LBB0_828
	v_cmp_le_u32_e64 s[14:15], s9, v90
	v_cmp_le_u32_e64 s[16:17], s9, v88
	v_cmp_le_u32_e64 s[18:19], s9, v89
	v_cmp_le_u32_e64 s[20:21], s9, v86
	v_cmp_le_u32_e64 s[22:23], s9, v87
	v_cmp_le_u32_e64 s[24:25], s9, v84
	v_cmp_le_u32_e64 s[26:27], s9, v85
	v_cmp_le_u32_e64 s[28:29], s9, v82
	v_cmp_le_u32_e64 s[30:31], s9, v83
	v_cmp_le_u32_e64 s[34:35], s9, v80
	v_cmp_le_u32_e64 s[36:37], s9, v81
	v_cmp_le_u32_e64 s[38:39], s9, v9
	s_bcnt1_i32_b64 s0, s[14:15]
	s_bcnt1_i32_b64 s1, s[16:17]
	s_add_i32 s0, s0, s1
	s_bcnt1_i32_b64 s1, s[18:19]
	s_add_i32 s0, s0, s1
	s_bcnt1_i32_b64 s1, s[20:21]
	s_add_i32 s0, s0, s1
	s_bcnt1_i32_b64 s1, s[22:23]
	s_add_i32 s0, s0, s1
	s_bcnt1_i32_b64 s1, s[24:25]
	s_add_i32 s0, s0, s1
	v_cmp_le_u32_e64 s[14:15], s9, v78
	v_cmp_le_u32_e64 s[16:17], s9, v7
	v_cmp_le_u32_e64 s[18:19], s9, v8
	v_cmp_le_u32_e64 s[20:21], s9, v5
	s_bcnt1_i32_b64 s1, s[26:27]
	s_add_i32 s0, s0, s1
	s_bcnt1_i32_b64 s1, s[28:29]
	s_add_i32 s0, s0, s1
	s_bcnt1_i32_b64 s1, s[30:31]
	s_add_i32 s0, s0, s1
	s_bcnt1_i32_b64 s1, s[34:35]
	s_add_i32 s0, s0, s1
	s_bcnt1_i32_b64 s1, s[36:37]
	s_add_i32 s0, s0, s1
	s_bcnt1_i32_b64 s1, s[38:39]
	s_add_i32 s0, s0, s1
	s_bcnt1_i32_b64 s1, s[14:15]
	s_add_i32 s0, s0, s1
	s_bcnt1_i32_b64 s1, s[16:17]
	s_add_i32 s0, s0, s1
	s_bcnt1_i32_b64 s1, s[18:19]
	s_add_i32 s0, s0, s1
	s_bcnt1_i32_b64 s1, s[20:21]
	s_add_i32 s0, s0, s1
	s_cmpk_eq_i32 s0, 0x100
	s_cbranch_scc1 .LBB0_832
	s_mov_b32 s0, 15
.LBB0_831:
	s_lshl_b32 s1, 1, s0
	s_or_b32 s1, s1, s9
	v_cmp_le_u32_e64 s[14:15], s1, v90
	v_cmp_le_u32_e64 s[16:17], s1, v88
	v_cmp_le_u32_e64 s[18:19], s1, v89
	v_cmp_le_u32_e64 s[20:21], s1, v86
	v_cmp_le_u32_e64 s[22:23], s1, v87
	v_cmp_le_u32_e64 s[24:25], s1, v84
	v_cmp_le_u32_e64 s[26:27], s1, v85
	v_cmp_le_u32_e64 s[28:29], s1, v82
	v_cmp_le_u32_e64 s[30:31], s1, v83
	v_cmp_le_u32_e64 s[34:35], s1, v80
	v_cmp_le_u32_e64 s[36:37], s1, v81
	v_cmp_le_u32_e64 s[38:39], s1, v9
	s_bcnt1_i32_b64 s11, s[14:15]
	s_bcnt1_i32_b64 s12, s[16:17]
	s_add_i32 s11, s11, s12
	s_bcnt1_i32_b64 s12, s[18:19]
	s_add_i32 s11, s11, s12
	s_bcnt1_i32_b64 s12, s[20:21]
	s_add_i32 s11, s11, s12
	s_bcnt1_i32_b64 s12, s[22:23]
	s_add_i32 s11, s11, s12
	s_bcnt1_i32_b64 s12, s[24:25]
	s_add_i32 s11, s11, s12
	v_cmp_le_u32_e64 s[14:15], s1, v78
	v_cmp_le_u32_e64 s[16:17], s1, v7
	v_cmp_le_u32_e64 s[18:19], s1, v8
	v_cmp_le_u32_e64 s[20:21], s1, v5
	s_bcnt1_i32_b64 s12, s[26:27]
	s_add_i32 s11, s11, s12
	s_bcnt1_i32_b64 s12, s[28:29]
	s_add_i32 s11, s11, s12
	s_bcnt1_i32_b64 s12, s[30:31]
	s_add_i32 s11, s11, s12
	s_bcnt1_i32_b64 s12, s[34:35]
	s_add_i32 s11, s11, s12
	s_bcnt1_i32_b64 s12, s[36:37]
	s_add_i32 s11, s11, s12
	s_bcnt1_i32_b64 s12, s[38:39]
	s_add_i32 s11, s11, s12
	s_bcnt1_i32_b64 s12, s[14:15]
	s_add_i32 s11, s11, s12
	s_bcnt1_i32_b64 s12, s[16:17]
	s_add_i32 s11, s11, s12
	s_bcnt1_i32_b64 s12, s[18:19]
	s_add_i32 s11, s11, s12
	s_bcnt1_i32_b64 s12, s[20:21]
	s_add_i32 s11, s11, s12
	s_cmpk_gt_u32 s11, 0xff
	s_cselect_b32 s9, s1, s9
	s_add_i32 s0, s0, -1
	s_cmp_eq_u32 s0, -1
	s_cbranch_scc0 .LBB0_831

.LBB0_875:
	s_add_i32 s0, s0, -1
	s_lshl_b32 s1, 1, s0
	s_or_b32 s1, s1, s10
	s_waitcnt lgkmcnt(0)
	v_cmp_le_u32_e64 s[14:15], s1, v90
	v_cmp_le_u32_e64 s[16:17], s1, v88
	v_cmp_le_u32_e64 s[18:19], s1, v89
	v_cmp_le_u32_e64 s[20:21], s1, v86
	v_cmp_le_u32_e64 s[22:23], s1, v87
	v_cmp_le_u32_e64 s[24:25], s1, v84
	v_cmp_le_u32_e64 s[26:27], s1, v85
	v_cmp_le_u32_e64 s[28:29], s1, v82
	v_cmp_le_u32_e64 s[30:31], s1, v83
	v_cmp_le_u32_e64 s[34:35], s1, v80
	v_cmp_le_u32_e64 s[36:37], s1, v81
	v_cmp_le_u32_e64 s[38:39], s1, v9
	s_bcnt1_i32_b64 s9, s[14:15]
	s_bcnt1_i32_b64 s11, s[16:17]
	s_add_i32 s9, s9, s11
	s_bcnt1_i32_b64 s11, s[18:19]
	s_add_i32 s9, s9, s11
	s_bcnt1_i32_b64 s11, s[20:21]
	s_add_i32 s9, s9, s11
	s_bcnt1_i32_b64 s11, s[22:23]
	s_add_i32 s9, s9, s11
	s_bcnt1_i32_b64 s11, s[24:25]
	s_add_i32 s9, s9, s11
	s_bcnt1_i32_b64 s11, s[26:27]
	s_add_i32 s9, s9, s11
	s_bcnt1_i32_b64 s11, s[28:29]
	s_add_i32 s9, s9, s11
	s_bcnt1_i32_b64 s11, s[30:31]
	s_add_i32 s9, s9, s11
	s_bcnt1_i32_b64 s11, s[34:35]
	s_add_i32 s9, s9, s11
	s_bcnt1_i32_b64 s11, s[36:37]
	s_add_i32 s9, s9, s11
	s_bcnt1_i32_b64 s11, s[38:39]
	s_add_i32 s9, s9, s11
	s_cmpk_gt_u32 s9, 0xff
	s_cselect_b32 s10, s1, s10
	s_cmp_lt_u32 s0, 17
	s_cbranch_scc0 .LBB0_875
	v_cmp_le_u32_e64 s[14:15], s10, v90
	v_cmp_le_u32_e64 s[16:17], s10, v88
	v_cmp_le_u32_e64 s[18:19], s10, v89
	v_cmp_le_u32_e64 s[20:21], s10, v86
	v_cmp_le_u32_e64 s[22:23], s10, v87
	v_cmp_le_u32_e64 s[24:25], s10, v84
	v_cmp_le_u32_e64 s[26:27], s10, v85
	v_cmp_le_u32_e64 s[28:29], s10, v82
	v_cmp_le_u32_e64 s[30:31], s10, v83
	v_cmp_le_u32_e64 s[34:35], s10, v80
	v_cmp_le_u32_e64 s[36:37], s10, v81
	v_cmp_le_u32_e64 s[38:39], s10, v9
	s_bcnt1_i32_b64 s0, s[14:15]
	s_bcnt1_i32_b64 s1, s[16:17]
	s_add_i32 s0, s0, s1
	s_bcnt1_i32_b64 s1, s[18:19]
	s_add_i32 s0, s0, s1
	s_bcnt1_i32_b64 s1, s[20:21]
	s_add_i32 s0, s0, s1
	s_bcnt1_i32_b64 s1, s[22:23]
	s_add_i32 s0, s0, s1
	s_bcnt1_i32_b64 s1, s[24:25]
	s_add_i32 s0, s0, s1
	s_bcnt1_i32_b64 s1, s[26:27]
	s_add_i32 s0, s0, s1
	s_bcnt1_i32_b64 s1, s[28:29]
	s_add_i32 s0, s0, s1
	s_bcnt1_i32_b64 s1, s[30:31]
	s_add_i32 s0, s0, s1
	s_bcnt1_i32_b64 s1, s[34:35]
	s_add_i32 s0, s0, s1
	s_bcnt1_i32_b64 s1, s[36:37]
	s_add_i32 s0, s0, s1
	s_bcnt1_i32_b64 s1, s[38:39]
	s_add_i32 s0, s0, s1
	s_cmpk_eq_i32 s0, 0x100
	s_cbranch_scc1 .LBB0_879
	s_mov_b32 s0, 15
.LBB0_878:
	s_lshl_b32 s1, 1, s0
	s_or_b32 s1, s1, s10
	v_cmp_le_u32_e64 s[14:15], s1, v90
	v_cmp_le_u32_e64 s[16:17], s1, v88
	v_cmp_le_u32_e64 s[18:19], s1, v89
	v_cmp_le_u32_e64 s[20:21], s1, v86
	v_cmp_le_u32_e64 s[22:23], s1, v87
	v_cmp_le_u32_e64 s[24:25], s1, v84
	v_cmp_le_u32_e64 s[26:27], s1, v85
	v_cmp_le_u32_e64 s[28:29], s1, v82
	v_cmp_le_u32_e64 s[30:31], s1, v83
	v_cmp_le_u32_e64 s[34:35], s1, v80
	v_cmp_le_u32_e64 s[36:37], s1, v81
	v_cmp_le_u32_e64 s[38:39], s1, v9
	s_bcnt1_i32_b64 s9, s[14:15]
	s_bcnt1_i32_b64 s11, s[16:17]
	s_add_i32 s9, s9, s11
	s_bcnt1_i32_b64 s11, s[18:19]
	s_add_i32 s9, s9, s11
	s_bcnt1_i32_b64 s11, s[20:21]
	s_add_i32 s9, s9, s11
	s_bcnt1_i32_b64 s11, s[22:23]
	s_add_i32 s9, s9, s11
	s_bcnt1_i32_b64 s11, s[24:25]
	s_add_i32 s9, s9, s11
	s_bcnt1_i32_b64 s11, s[26:27]
	s_add_i32 s9, s9, s11
	s_bcnt1_i32_b64 s11, s[28:29]
	s_add_i32 s9, s9, s11
	s_bcnt1_i32_b64 s11, s[30:31]
	s_add_i32 s9, s9, s11
	s_bcnt1_i32_b64 s11, s[34:35]
	s_add_i32 s9, s9, s11
	s_bcnt1_i32_b64 s11, s[36:37]
	s_add_i32 s9, s9, s11
	s_bcnt1_i32_b64 s11, s[38:39]
	s_add_i32 s9, s9, s11
	s_cmpk_gt_u32 s9, 0xff
	s_cselect_b32 s10, s1, s10
	s_add_i32 s0, s0, -1
	s_cmp_eq_u32 s0, -1
	s_cbranch_scc0 .LBB0_878
